# speedup vs baseline: 1.0453x; 1.0033x over previous
_ZN12_GLOBAL__N_18k_layer1EPKDF16_PKfS3_PKiPK15HIP_vector_typeIjLj4EES1_S3_S1_S3_S3_PDF16_PfSB_S3_:
	s_load_dwordx2 s[6:7], s[0:1], 0x18
	s_load_dwordx2 s[20:21], s[0:1], 0x0
	s_load_dwordx2 s[28:29], s[0:1], 0x8
	s_load_dwordx2 s[30:31], s[0:1], 0x20
	s_load_dwordx2 s[24:25], s[0:1], 0x68
	s_load_dwordx2 s[14:15], s[0:1], 0x48
	s_load_dwordx4 s[16:19], s[0:1], 0x38
	s_load_dwordx2 s[34:35], s[0:1], 0x10
	s_load_dwordx2 s[26:27], s[0:1], 0x28
	v_readfirstlane_b32 s43, v0
	s_lshl_b32 s33, s2, 4
	v_cmp_gt_u32_e32 vcc, 16, v0
	v_lshlrev_b32_e32 v1, 2, v0
	s_and_saveexec_b64 s[2:3], vcc
	s_cbranch_execz .LBB2_2
	v_or_b32_e32 v2, s33, v0
	v_ashrrev_i32_e32 v3, 31, v2
	s_waitcnt lgkmcnt(0)
	v_lshl_add_u64 v[2:3], v[2:3], 2, s[6:7]
	global_load_dwordx2 v[2:3], v[2:3], off
	s_waitcnt vmcnt(0)
	v_sub_u32_e32 v3, v3, v2
	ds_write_b32 v1, v2 offset:16640
	ds_write_b32 v1, v3 offset:25088
.LBB2_2:
	s_or_b64 exec, exec, s[2:3]
	s_waitcnt lgkmcnt(0)
	s_barrier
	s_and_saveexec_b64 s[8:9], vcc
	s_cbranch_execz .LBB2_4
	ds_read_b32 v1, v1 offset:25088
	v_mov_b32_e32 v14, 0
	ds_read_b128 v[2:5], v14 offset:25088
	ds_read_b128 v[6:9], v14 offset:25104
	ds_read_b128 v[10:13], v14 offset:25120
	ds_read_b128 v[14:17], v14 offset:25136
	v_cmp_ne_u32_e64 s[4:5], 0, v0
	s_waitcnt lgkmcnt(3)
	v_cmp_eq_u32_e64 s[2:3], v2, v1
	v_cmp_lt_i32_e32 vcc, v2, v1
	s_and_b64 s[2:3], s[2:3], s[4:5]
	s_or_b64 s[2:3], vcc, s[2:3]
	v_cndmask_b32_e64 v2, 0, 1, s[2:3]
	v_cmp_eq_u32_e64 s[2:3], v3, v1
	v_cmp_lt_u32_e64 s[4:5], 1, v0
	v_cmp_lt_i32_e32 vcc, v3, v1
	s_and_b64 s[2:3], s[2:3], s[4:5]
	s_or_b64 s[2:3], vcc, s[2:3]
	v_cndmask_b32_e64 v3, 0, 1, s[2:3]
	v_cmp_eq_u32_e64 s[2:3], v4, v1
	v_cmp_lt_u32_e64 s[4:5], 2, v0
	v_cmp_lt_i32_e32 vcc, v4, v1
	s_and_b64 s[2:3], s[2:3], s[4:5]
	s_or_b64 s[2:3], vcc, s[2:3]
	v_cndmask_b32_e64 v4, 0, 1, s[2:3]
	v_cmp_eq_u32_e64 s[2:3], v5, v1
	v_cmp_lt_u32_e64 s[4:5], 3, v0
	v_cmp_lt_i32_e32 vcc, v5, v1
	s_and_b64 s[2:3], s[2:3], s[4:5]
	s_or_b64 s[2:3], vcc, s[2:3]
	v_cndmask_b32_e64 v5, 0, 1, s[2:3]
	s_waitcnt lgkmcnt(2)
	v_cmp_eq_u32_e64 s[2:3], v6, v1
	v_cmp_lt_u32_e64 s[4:5], 4, v0
	v_cmp_lt_i32_e32 vcc, v6, v1
	s_and_b64 s[2:3], s[2:3], s[4:5]
	s_or_b64 s[2:3], vcc, s[2:3]
	v_cndmask_b32_e64 v6, 0, 1, s[2:3]
	v_cmp_eq_u32_e64 s[2:3], v7, v1
	v_cmp_lt_u32_e64 s[4:5], 5, v0
	v_cmp_lt_i32_e32 vcc, v7, v1
	s_and_b64 s[2:3], s[2:3], s[4:5]
	s_or_b64 s[2:3], vcc, s[2:3]
	v_cndmask_b32_e64 v7, 0, 1, s[2:3]
	v_cmp_eq_u32_e64 s[2:3], v8, v1
	v_cmp_lt_u32_e64 s[4:5], 6, v0
	v_cmp_lt_i32_e32 vcc, v8, v1
	s_and_b64 s[2:3], s[2:3], s[4:5]
	s_or_b64 s[2:3], vcc, s[2:3]
	v_cndmask_b32_e64 v8, 0, 1, s[2:3]
	v_cmp_eq_u32_e64 s[2:3], v9, v1
	v_cmp_lt_u32_e64 s[4:5], 7, v0
	v_cmp_lt_i32_e32 vcc, v9, v1
	s_and_b64 s[2:3], s[2:3], s[4:5]
	s_or_b64 s[2:3], vcc, s[2:3]
	v_cndmask_b32_e64 v9, 0, 1, s[2:3]
	s_waitcnt lgkmcnt(1)
	v_cmp_eq_u32_e64 s[2:3], v10, v1
	v_cmp_lt_u32_e64 s[4:5], 8, v0
	v_cmp_lt_i32_e32 vcc, v10, v1
	s_and_b64 s[2:3], s[2:3], s[4:5]
	s_or_b64 s[2:3], vcc, s[2:3]
	v_cndmask_b32_e64 v10, 0, 1, s[2:3]
	v_cmp_eq_u32_e64 s[2:3], v11, v1
	v_cmp_lt_u32_e64 s[4:5], 9, v0
	v_cmp_lt_i32_e32 vcc, v11, v1
	s_and_b64 s[2:3], s[2:3], s[4:5]
	s_or_b64 s[2:3], vcc, s[2:3]
	v_cndmask_b32_e64 v11, 0, 1, s[2:3]
	v_cmp_eq_u32_e64 s[2:3], v12, v1
	v_cmp_lt_u32_e64 s[4:5], 10, v0
	v_cmp_lt_i32_e32 vcc, v12, v1
	s_and_b64 s[2:3], s[2:3], s[4:5]
	s_or_b64 s[2:3], vcc, s[2:3]
	v_cndmask_b32_e64 v12, 0, 1, s[2:3]
	v_cmp_eq_u32_e64 s[2:3], v13, v1
	v_cmp_lt_u32_e64 s[4:5], 11, v0
	v_cmp_lt_i32_e32 vcc, v13, v1
	s_and_b64 s[2:3], s[2:3], s[4:5]
	s_or_b64 s[2:3], vcc, s[2:3]
	v_cndmask_b32_e64 v13, 0, 1, s[2:3]
	s_waitcnt lgkmcnt(0)
	v_cmp_eq_u32_e64 s[2:3], v14, v1
	v_cmp_lt_u32_e64 s[4:5], 12, v0
	v_cmp_lt_i32_e32 vcc, v14, v1
	s_and_b64 s[2:3], s[2:3], s[4:5]
	s_or_b64 s[2:3], vcc, s[2:3]
	v_lshlrev_b32_e32 v2, 2, v2
	v_cndmask_b32_e64 v14, 0, 1, s[2:3]
	v_cmp_eq_u32_e64 s[2:3], v15, v1
	v_cmp_lt_u32_e64 s[4:5], 13, v0
	v_lshl_add_u32 v2, v3, 2, v2
	v_cmp_lt_i32_e32 vcc, v15, v1
	s_and_b64 s[2:3], s[2:3], s[4:5]
	v_lshl_add_u32 v2, v4, 2, v2
	s_or_b64 s[2:3], vcc, s[2:3]
	v_lshl_add_u32 v2, v5, 2, v2
	v_lshlrev_b32_e32 v3, 2, v6
	v_lshlrev_b32_e32 v4, 2, v7
	v_cndmask_b32_e64 v15, 0, 1, s[2:3]
	v_cmp_eq_u32_e64 s[2:3], v16, v1
	v_cmp_eq_u32_e64 s[4:5], 15, v0
	v_add3_u32 v2, v3, v2, v4
	v_lshlrev_b32_e32 v3, 2, v8
	v_lshlrev_b32_e32 v4, 2, v9
	v_cmp_lt_i32_e32 vcc, v16, v1
	s_and_b64 s[2:3], s[2:3], s[4:5]
	v_add3_u32 v2, v2, v3, v4
	v_lshlrev_b32_e32 v3, 2, v10
	v_lshlrev_b32_e32 v4, 2, v11
	s_or_b64 s[2:3], vcc, s[2:3]
	v_cmp_lt_i32_e32 vcc, v17, v1
	v_add3_u32 v2, v2, v3, v4
	v_lshlrev_b32_e32 v3, 2, v12
	v_lshlrev_b32_e32 v4, 2, v13
	v_cndmask_b32_e64 v16, 0, 1, s[2:3]
	v_cndmask_b32_e64 v1, 0, 1, vcc
	v_add3_u32 v2, v2, v3, v4
	v_lshlrev_b32_e32 v3, 2, v14
	v_lshlrev_b32_e32 v4, 2, v15
	v_add3_u32 v2, v2, v3, v4
	v_lshlrev_b32_e32 v3, 2, v16
	v_lshlrev_b32_e32 v1, 2, v1
	v_add3_u32 v1, v2, v3, v1
	ds_write_b32 v1, v0 offset:25152
.LBB2_4:
	s_or_b64 exec, exec, s[8:9]
	s_lshr_b32 s41, s43, 6
	v_bfe_u32 v1, v0, 4, 2
	s_lshl_b32 s45, s41, 2
	v_or_b32_e32 v41, s45, v1
	v_lshlrev_b32_e32 v2, 2, v41
	s_waitcnt lgkmcnt(0)
	s_barrier
	ds_read_b32 v2, v2 offset:25152
	s_and_b32 s44, s21, 0xffff
	v_and_b32_e32 v68, 63, v0
	s_mov_b32 s23, 0x20000
	s_mov_b32 s22, 0x4e2000
	s_waitcnt lgkmcnt(0)
	v_add_u32_e32 v34, s33, v2
	v_lshlrev_b32_e32 v3, 2, v2
	ds_read_b32 v36, v3 offset:16640
	ds_read_b32 v35, v3 offset:25088
	s_mov_b64 s[2:3], -1
	s_waitcnt lgkmcnt(0)
	v_add_u32_e32 v37, v36, v35
	v_cmp_gt_i32_e32 vcc, 48, v35
	s_cmp_eq_u64 vcc, exec
	s_cbranch_scc1 .LBB2_25
	v_mov_b32_e32 v7, 0
	v_lshlrev_b32_e32 v8, 2, v68
	v_mov_b32_e32 v9, v7
	v_lshl_add_u64 v[10:11], s[20:21], 0, v[8:9]
	s_mov_b32 s46, 0
	s_branch .LBB2_7

.LBB2_57:
	s_endpgm
	s_nop 0
	s_nop 0
	s_nop 0
	s_nop 0
	s_nop 0
	s_nop 0
	s_nop 0
	s_nop 0
	s_nop 0
	s_nop 0
	s_nop 0
	s_nop 0
	s_nop 0
	s_nop 0
	s_nop 0
	s_nop 0
	s_nop 0
	s_nop 0
	s_nop 0
	s_nop 0
	s_nop 0
	s_nop 0
	s_nop 0
	s_nop 0
	s_nop 0
	s_nop 0
	s_nop 0
	s_nop 0
	s_nop 0
	s_nop 0
	s_nop 0
	s_nop 0
	s_nop 0
	s_endpgm
